# speedup vs baseline: 1.0104x; 1.0104x over previous
.LBB1_3:
	ds_read_b128 v[128:131], v126 offset:49152
	ds_read_b128 v[132:135], v126 offset:50176
	ds_read_b128 v[136:139], v126 offset:51200
	ds_read_b128 v[140:143], v126 offset:52224
	s_add_u32 s30, s16, s0
	s_addc_u32 s31, s17, s1
	ds_read_b128 v[144:147], v110
	ds_read_b128 v[148:151], v110 offset:1024
	ds_read_b128 v[152:155], v109
	ds_read_b128 v[156:159], v109 offset:1024
	ds_read_b128 v[160:163], v108
	ds_read_b128 v[164:167], v108 offset:1024
	v_readfirstlane_b32 s34, v127
	s_add_u32 s52, s30, s18
	s_addc_u32 s53, s31, s19
	s_mov_b32 m0, s34
	s_nop 0
	global_load_lds_dwordx4 v100, s[52:53]
	v_readfirstlane_b32 s34, v125
	s_add_u32 s52, s30, s18
	s_addc_u32 s53, s31, s19
	s_mov_b32 m0, s34
	s_nop 0
	global_load_lds_dwordx4 v101, s[52:53]
	s_waitcnt lgkmcnt(6)
	s_barrier
	s_waitcnt lgkmcnt(0)
	s_setprio 0
	s_waitcnt lgkmcnt(0)
	v_mfma_f32_16x16x32_f16 v[94:97], v[144:147], v[128:131], v[94:97]
	v_mfma_f32_16x16x32_f16 v[90:93], v[144:147], v[136:139], v[90:93]
	v_mfma_f32_16x16x32_f16 v[86:89], v[152:155], v[128:131], v[86:89]
	v_mfma_f32_16x16x32_f16 v[82:85], v[152:155], v[136:139], v[82:85]
	v_mfma_f32_16x16x32_f16 v[78:81], v[160:163], v[128:131], v[78:81]
	v_mfma_f32_16x16x32_f16 v[74:77], v[160:163], v[136:139], v[74:77]
	v_mfma_f32_16x16x32_f16 v[94:97], v[148:151], v[132:135], v[94:97]
	v_mfma_f32_16x16x32_f16 v[90:93], v[148:151], v[140:143], v[90:93]
	v_mfma_f32_16x16x32_f16 v[86:89], v[156:159], v[132:135], v[86:89]
	v_mfma_f32_16x16x32_f16 v[82:85], v[156:159], v[140:143], v[82:85]
	v_mfma_f32_16x16x32_f16 v[78:81], v[164:167], v[132:135], v[78:81]
	v_mfma_f32_16x16x32_f16 v[74:77], v[164:167], v[140:143], v[74:77]
	s_setprio 1
	s_barrier
	s_add_u32 s34, s2, s0
	s_addc_u32 s35, s3, s1
	ds_read_b128 v[168:171], v122
	ds_read_b128 v[172:175], v122 offset:1024
	ds_read_b128 v[176:179], v122 offset:2048
	ds_read_b128 v[180:183], v122 offset:3072
	v_readfirstlane_b32 s42, v106
	s_add_u32 s54, s34, s20
	s_addc_u32 s55, s35, s21
	s_mov_b32 m0, s42
	s_nop 0
	global_load_lds_dwordx4 v100, s[54:55]
	v_readfirstlane_b32 s42, v107
	s_add_u32 s54, s34, s20
	s_addc_u32 s55, s35, s21
	s_mov_b32 m0, s42
	s_nop 0
	global_load_lds_dwordx4 v103, s[54:55]
	s_barrier
	s_waitcnt lgkmcnt(0)
	s_setprio 0
	s_waitcnt lgkmcnt(0)
	v_mfma_f32_16x16x32_f16 v[70:73], v[144:147], v[168:171], v[70:73]
	v_mfma_f32_16x16x32_f16 v[66:69], v[144:147], v[176:179], v[66:69]
	v_mfma_f32_16x16x32_f16 v[62:65], v[152:155], v[168:171], v[62:65]
	v_mfma_f32_16x16x32_f16 v[50:53], v[152:155], v[176:179], v[50:53]
	v_mfma_f32_16x16x32_f16 v[46:49], v[160:163], v[168:171], v[46:49]
	v_mfma_f32_16x16x32_f16 v[42:45], v[160:163], v[176:179], v[42:45]
	v_mfma_f32_16x16x32_f16 v[70:73], v[148:151], v[172:175], v[70:73]
	v_mfma_f32_16x16x32_f16 v[66:69], v[148:151], v[180:183], v[66:69]
	v_mfma_f32_16x16x32_f16 v[62:65], v[156:159], v[172:175], v[62:65]
	v_mfma_f32_16x16x32_f16 v[50:53], v[156:159], v[180:183], v[50:53]
	v_mfma_f32_16x16x32_f16 v[46:49], v[164:167], v[172:175], v[46:49]
	v_mfma_f32_16x16x32_f16 v[42:45], v[164:167], v[180:183], v[42:45]
	s_setprio 1
	s_barrier
	ds_read_b128 v[144:147], v110 offset:12288
	ds_read_b128 v[148:151], v110 offset:13312
	ds_read_b128 v[152:155], v109 offset:12288
	ds_read_b128 v[156:159], v109 offset:13312
	ds_read_b128 v[160:163], v108 offset:12288
	ds_read_b128 v[164:167], v108 offset:13312
	v_readfirstlane_b32 s42, v1
	s_add_u32 s54, s30, s20
	s_addc_u32 s55, s31, s21
	s_mov_b32 m0, s42
	s_nop 0
	global_load_lds_dwordx4 v100, s[54:55]
	v_readfirstlane_b32 s42, v111
	s_add_u32 s54, s30, s20
	s_addc_u32 s55, s31, s21
	s_mov_b32 m0, s42
	s_nop 0
	global_load_lds_dwordx4 v101, s[54:55]
	s_barrier
	s_waitcnt lgkmcnt(0)
	s_setprio 0
	s_waitcnt lgkmcnt(0)
	v_mfma_f32_16x16x32_f16 v[38:41], v[144:147], v[128:131], v[38:41]
	v_mfma_f32_16x16x32_f16 v[34:37], v[144:147], v[136:139], v[34:37]
	v_mfma_f32_16x16x32_f16 v[30:33], v[152:155], v[128:131], v[30:33]
	v_mfma_f32_16x16x32_f16 v[26:29], v[152:155], v[136:139], v[26:29]
	v_mfma_f32_16x16x32_f16 v[22:25], v[160:163], v[128:131], v[22:25]
	v_mfma_f32_16x16x32_f16 v[18:21], v[160:163], v[136:139], v[18:21]
	v_mfma_f32_16x16x32_f16 v[38:41], v[148:151], v[132:135], v[38:41]
	v_mfma_f32_16x16x32_f16 v[34:37], v[148:151], v[140:143], v[34:37]
	v_mfma_f32_16x16x32_f16 v[30:33], v[156:159], v[132:135], v[30:33]
	v_mfma_f32_16x16x32_f16 v[26:29], v[156:159], v[140:143], v[26:29]
	v_mfma_f32_16x16x32_f16 v[22:25], v[164:167], v[132:135], v[22:25]
	v_mfma_f32_16x16x32_f16 v[18:21], v[164:167], v[140:143], v[18:21]
	s_setprio 1
	s_barrier
	v_readfirstlane_b32 s42, v112
	s_add_u32 s56, s34, s22
	s_addc_u32 s57, s35, s23
	s_mov_b32 m0, s42
	s_nop 0
	global_load_lds_dwordx4 v100, s[56:57]
	v_readfirstlane_b32 s42, v113
	s_add_u32 s56, s34, s22
	s_addc_u32 s57, s35, s23
	s_mov_b32 m0, s42
	s_nop 0
	global_load_lds_dwordx4 v103, s[56:57]
	s_waitcnt vmcnt(6)
	s_barrier
	s_setprio 0
	v_mfma_f32_16x16x32_f16 v[14:17], v[144:147], v[168:171], v[14:17]
	v_mfma_f32_16x16x32_f16 v[10:13], v[144:147], v[176:179], v[10:13]
	v_mfma_f32_16x16x32_f16 v[6:9], v[152:155], v[168:171], v[6:9]
	v_mfma_f32_16x16x32_f16 v[2:5], v[152:155], v[176:179], v[2:5]
	v_mfma_f32_16x16x32_f16 v[54:57], v[160:163], v[168:171], v[54:57]
	v_mfma_f32_16x16x32_f16 v[58:61], v[160:163], v[176:179], v[58:61]
	v_mfma_f32_16x16x32_f16 v[14:17], v[148:151], v[172:175], v[14:17]
	v_mfma_f32_16x16x32_f16 v[10:13], v[148:151], v[180:183], v[10:13]
	v_mfma_f32_16x16x32_f16 v[6:9], v[156:159], v[172:175], v[6:9]
	v_mfma_f32_16x16x32_f16 v[2:5], v[156:159], v[180:183], v[2:5]
	v_mfma_f32_16x16x32_f16 v[54:57], v[164:167], v[172:175], v[54:57]
	v_mfma_f32_16x16x32_f16 v[58:61], v[164:167], v[180:183], v[58:61]
	s_setprio 1
	s_barrier
	ds_read_b128 v[128:131], v117
	ds_read_b128 v[132:135], v117 offset:1024
	ds_read_b128 v[136:139], v117 offset:2048
	ds_read_b128 v[140:143], v117 offset:3072
	ds_read_b128 v[144:147], v110 offset:24576
	ds_read_b128 v[148:151], v110 offset:25600
	ds_read_b128 v[152:155], v109 offset:24576
	ds_read_b128 v[156:159], v109 offset:25600
	ds_read_b128 v[160:163], v108 offset:24576
	ds_read_b128 v[164:167], v108 offset:25600
	v_readfirstlane_b32 s42, v115
	s_add_u32 s52, s30, s24
	s_addc_u32 s53, s31, s25
	s_mov_b32 m0, s42
	s_nop 0
	global_load_lds_dwordx4 v100, s[52:53]
	v_readfirstlane_b32 s42, v116
	s_add_u32 s52, s30, s24
	s_addc_u32 s53, s31, s25
	s_mov_b32 m0, s42
	s_nop 0
	global_load_lds_dwordx4 v101, s[52:53]
	s_waitcnt lgkmcnt(6)
	s_barrier
	s_waitcnt lgkmcnt(0)
	s_setprio 0
	s_waitcnt lgkmcnt(0)
	v_mfma_f32_16x16x32_f16 v[94:97], v[144:147], v[128:131], v[94:97]
	v_mfma_f32_16x16x32_f16 v[90:93], v[144:147], v[136:139], v[90:93]
	v_mfma_f32_16x16x32_f16 v[86:89], v[152:155], v[128:131], v[86:89]
	v_mfma_f32_16x16x32_f16 v[82:85], v[152:155], v[136:139], v[82:85]
	v_mfma_f32_16x16x32_f16 v[78:81], v[160:163], v[128:131], v[78:81]
	v_mfma_f32_16x16x32_f16 v[74:77], v[160:163], v[136:139], v[74:77]
	v_mfma_f32_16x16x32_f16 v[94:97], v[148:151], v[132:135], v[94:97]
	v_mfma_f32_16x16x32_f16 v[90:93], v[148:151], v[140:143], v[90:93]
	v_mfma_f32_16x16x32_f16 v[86:89], v[156:159], v[132:135], v[86:89]
	v_mfma_f32_16x16x32_f16 v[82:85], v[156:159], v[140:143], v[82:85]
	v_mfma_f32_16x16x32_f16 v[78:81], v[164:167], v[132:135], v[78:81]
	v_mfma_f32_16x16x32_f16 v[74:77], v[164:167], v[140:143], v[74:77]
	s_setprio 1
	s_barrier
	ds_read_b128 v[168:171], v114
	ds_read_b128 v[172:175], v114 offset:1024
	ds_read_b128 v[176:179], v114 offset:2048
	ds_read_b128 v[180:183], v114 offset:3072
	v_readfirstlane_b32 s42, v118
	s_add_u32 s54, s34, s26
	s_addc_u32 s55, s35, s27
	s_mov_b32 m0, s42
	s_nop 0
	global_load_lds_dwordx4 v100, s[54:55]
	v_readfirstlane_b32 s42, v119
	s_add_u32 s54, s34, s26
	s_addc_u32 s55, s35, s27
	s_mov_b32 m0, s42
	s_nop 0
	global_load_lds_dwordx4 v103, s[54:55]
	s_barrier
	s_waitcnt lgkmcnt(0)
	s_setprio 0
	s_waitcnt lgkmcnt(0)
	v_mfma_f32_16x16x32_f16 v[70:73], v[144:147], v[168:171], v[70:73]
	v_mfma_f32_16x16x32_f16 v[66:69], v[144:147], v[176:179], v[66:69]
	v_mfma_f32_16x16x32_f16 v[62:65], v[152:155], v[168:171], v[62:65]
	v_mfma_f32_16x16x32_f16 v[50:53], v[152:155], v[176:179], v[50:53]
	v_mfma_f32_16x16x32_f16 v[46:49], v[160:163], v[168:171], v[46:49]
	v_mfma_f32_16x16x32_f16 v[42:45], v[160:163], v[176:179], v[42:45]
	v_mfma_f32_16x16x32_f16 v[70:73], v[148:151], v[172:175], v[70:73]
	v_mfma_f32_16x16x32_f16 v[66:69], v[148:151], v[180:183], v[66:69]
	v_mfma_f32_16x16x32_f16 v[62:65], v[156:159], v[172:175], v[62:65]
	v_mfma_f32_16x16x32_f16 v[50:53], v[156:159], v[180:183], v[50:53]
	v_mfma_f32_16x16x32_f16 v[46:49], v[164:167], v[172:175], v[46:49]
	v_mfma_f32_16x16x32_f16 v[42:45], v[164:167], v[180:183], v[42:45]
	s_setprio 1
	s_barrier
	ds_read_b128 v[144:147], v110 offset:36864
	ds_read_b128 v[148:151], v110 offset:37888
	ds_read_b128 v[152:155], v109 offset:36864
	ds_read_b128 v[156:159], v109 offset:37888
	ds_read_b128 v[160:163], v108 offset:36864
	ds_read_b128 v[164:167], v108 offset:37888
	v_readfirstlane_b32 s42, v120
	s_add_u32 s54, s30, s26
	s_addc_u32 s55, s31, s27
	s_mov_b32 m0, s42
	s_nop 0
	global_load_lds_dwordx4 v100, s[54:55]
	s_nop 0
	s_add_u32 s54, s30, s26
	s_addc_u32 s55, s31, s27
	v_readfirstlane_b32 s30, v121
	s_mov_b32 m0, s30
	s_nop 0
	global_load_lds_dwordx4 v101, s[54:55]
	s_barrier
	s_waitcnt lgkmcnt(0)
	s_setprio 0
	s_waitcnt lgkmcnt(0)
	v_mfma_f32_16x16x32_f16 v[38:41], v[144:147], v[128:131], v[38:41]
	v_mfma_f32_16x16x32_f16 v[34:37], v[144:147], v[136:139], v[34:37]
	v_mfma_f32_16x16x32_f16 v[30:33], v[152:155], v[128:131], v[30:33]
	v_mfma_f32_16x16x32_f16 v[26:29], v[152:155], v[136:139], v[26:29]
	v_mfma_f32_16x16x32_f16 v[22:25], v[160:163], v[128:131], v[22:25]
	v_mfma_f32_16x16x32_f16 v[18:21], v[160:163], v[136:139], v[18:21]
	v_mfma_f32_16x16x32_f16 v[38:41], v[148:151], v[132:135], v[38:41]
	v_mfma_f32_16x16x32_f16 v[34:37], v[148:151], v[140:143], v[34:37]
	v_mfma_f32_16x16x32_f16 v[30:33], v[156:159], v[132:135], v[30:33]
	v_mfma_f32_16x16x32_f16 v[26:29], v[156:159], v[140:143], v[26:29]
	v_mfma_f32_16x16x32_f16 v[22:25], v[164:167], v[132:135], v[22:25]
	v_mfma_f32_16x16x32_f16 v[18:21], v[164:167], v[140:143], v[18:21]
	s_setprio 1
	s_barrier
	v_readfirstlane_b32 s30, v123
	s_add_u32 s56, s34, s28
	s_addc_u32 s57, s35, s29
	s_mov_b32 m0, s30
	s_nop 0
	global_load_lds_dwordx4 v100, s[56:57]
	v_readfirstlane_b32 s30, v124
	s_add_u32 s56, s34, s28
	s_addc_u32 s57, s35, s29
	s_mov_b32 m0, s30
	s_nop 0
	global_load_lds_dwordx4 v103, s[56:57]
	s_waitcnt vmcnt(6)
	s_barrier
	s_setprio 0
	v_mfma_f32_16x16x32_f16 v[14:17], v[144:147], v[168:171], v[14:17]
	v_mfma_f32_16x16x32_f16 v[10:13], v[144:147], v[176:179], v[10:13]
	v_mfma_f32_16x16x32_f16 v[6:9], v[152:155], v[168:171], v[6:9]
	v_mfma_f32_16x16x32_f16 v[2:5], v[152:155], v[176:179], v[2:5]
	v_mfma_f32_16x16x32_f16 v[54:57], v[160:163], v[168:171], v[54:57]
	v_mfma_f32_16x16x32_f16 v[58:61], v[160:163], v[176:179], v[58:61]
	v_mfma_f32_16x16x32_f16 v[14:17], v[148:151], v[172:175], v[14:17]
	v_mfma_f32_16x16x32_f16 v[10:13], v[148:151], v[180:183], v[10:13]
	v_mfma_f32_16x16x32_f16 v[6:9], v[156:159], v[172:175], v[6:9]
	v_mfma_f32_16x16x32_f16 v[2:5], v[156:159], v[180:183], v[2:5]
	v_mfma_f32_16x16x32_f16 v[54:57], v[164:167], v[172:175], v[54:57]
	v_mfma_f32_16x16x32_f16 v[58:61], v[164:167], v[180:183], v[58:61]
	s_setprio 1
	s_add_i32 s41, s41, 2
	s_add_u32 s0, s0, 0x100
	s_addc_u32 s1, s1, 0
	s_cmp_lt_u32 s41, 12
	s_barrier
	s_cbranch_scc1 .LBB1_3
	v_add_u32_e32 v98, 0x9000, v1
	s_add_u32 s0, s16, 0x30780
	v_readfirstlane_b32 s2, v98
	s_addc_u32 s1, s17, 0
	s_mov_b32 m0, s2
	v_readfirstlane_b32 s2, v125
	ds_read_b128 v[118:121], v126 offset:49152
	ds_read_b128 v[128:131], v126 offset:50176
	ds_read_b128 v[132:135], v126 offset:51200
	ds_read_b128 v[136:139], v126 offset:52224
	ds_read_b128 v[140:143], v110
	ds_read_b128 v[144:147], v110 offset:1024
	ds_read_b128 v[148:151], v109
	ds_read_b128 v[152:155], v109 offset:1024
	ds_read_b128 v[156:159], v108
	ds_read_b128 v[160:163], v108 offset:1024
	s_nop 0
	global_load_lds_dwordx4 v100, s[0:1]
	s_mov_b32 m0, s2
	s_nop 0
	global_load_lds_dwordx4 v101, s[0:1]
	s_barrier
	s_waitcnt lgkmcnt(0)
	s_setprio 0
	s_waitcnt lgkmcnt(0)
	v_mfma_f32_16x16x32_f16 v[90:93], v[140:143], v[132:135], v[90:93]
	v_mfma_f32_16x16x32_f16 v[86:89], v[148:151], v[118:121], v[86:89]
	v_mfma_f32_16x16x32_f16 v[82:85], v[148:151], v[132:135], v[82:85]
	v_mfma_f32_16x16x32_f16 v[94:97], v[140:143], v[118:121], v[94:97]
	v_mfma_f32_16x16x32_f16 v[90:93], v[144:147], v[136:139], v[90:93]
	v_mfma_f32_16x16x32_f16 v[86:89], v[152:155], v[128:131], v[86:89]
	v_mfma_f32_16x16x32_f16 v[82:85], v[152:155], v[136:139], v[82:85]
	v_mfma_f32_16x16x32_f16 v[78:81], v[156:159], v[118:121], v[78:81]
	v_mfma_f32_16x16x32_f16 v[74:77], v[156:159], v[132:135], v[74:77]
	v_mfma_f32_16x16x32_f16 v[94:97], v[144:147], v[128:131], v[94:97]
	v_mfma_f32_16x16x32_f16 v[124:127], v[160:163], v[128:131], v[78:81]
	v_mfma_f32_16x16x32_f16 v[164:167], v[160:163], v[136:139], v[74:77]
	s_setprio 1
	s_barrier
	s_nop 2
	ds_read_b128 v[74:77], v122
	ds_read_b128 v[78:81], v122 offset:1024
	ds_read_b128 v[98:101], v122 offset:2048
	ds_read_b128 v[168:171], v122 offset:3072
	s_barrier
	s_waitcnt lgkmcnt(0)
	s_setprio 0
	s_waitcnt lgkmcnt(0)
	v_mfma_f32_16x16x32_f16 v[70:73], v[140:143], v[74:77], v[70:73]
	v_mfma_f32_16x16x32_f16 v[66:69], v[140:143], v[98:101], v[66:69]
	v_mfma_f32_16x16x32_f16 v[50:53], v[148:151], v[98:101], v[50:53]
	v_mfma_f32_16x16x32_f16 v[46:49], v[156:159], v[74:77], v[46:49]
	v_mfma_f32_16x16x32_f16 v[42:45], v[156:159], v[98:101], v[42:45]
	v_mfma_f32_16x16x32_f16 v[70:73], v[144:147], v[78:81], v[70:73]
	v_mfma_f32_16x16x32_f16 v[66:69], v[144:147], v[168:171], v[66:69]
	v_mfma_f32_16x16x32_f16 v[62:65], v[148:151], v[74:77], v[62:65]
	v_mfma_f32_16x16x32_f16 v[50:53], v[152:155], v[168:171], v[50:53]
	v_mfma_f32_16x16x32_f16 v[46:49], v[160:163], v[78:81], v[46:49]
	v_mfma_f32_16x16x32_f16 v[42:45], v[160:163], v[168:171], v[42:45]
	v_mfma_f32_16x16x32_f16 v[140:143], v[152:155], v[78:81], v[62:65]
	s_setprio 1
	s_barrier
	s_nop 1
	ds_read_b128 v[62:65], v110 offset:12288
	ds_read_b128 v[144:147], v110 offset:13312
	ds_read_b128 v[148:151], v109 offset:12288
	ds_read_b128 v[152:155], v109 offset:13312
	ds_read_b128 v[156:159], v108 offset:12288
	ds_read_b128 v[160:163], v108 offset:13312
	s_waitcnt vmcnt(4)
	s_barrier
	s_waitcnt lgkmcnt(0)
	s_setprio 0
	s_waitcnt lgkmcnt(0)
	v_mfma_f32_16x16x32_f16 v[38:41], v[62:65], v[118:121], v[38:41]
	v_mfma_f32_16x16x32_f16 v[34:37], v[62:65], v[132:135], v[34:37]
	v_mfma_f32_16x16x32_f16 v[30:33], v[148:151], v[118:121], v[30:33]
	v_mfma_f32_16x16x32_f16 v[26:29], v[148:151], v[132:135], v[26:29]
	v_mfma_f32_16x16x32_f16 v[22:25], v[156:159], v[118:121], v[22:25]
	v_mfma_f32_16x16x32_f16 v[18:21], v[156:159], v[132:135], v[18:21]
	v_mfma_f32_16x16x32_f16 v[38:41], v[144:147], v[128:131], v[38:41]
	v_mfma_f32_16x16x32_f16 v[34:37], v[144:147], v[136:139], v[34:37]
	v_mfma_f32_16x16x32_f16 v[30:33], v[152:155], v[128:131], v[30:33]
	v_mfma_f32_16x16x32_f16 v[26:29], v[152:155], v[136:139], v[26:29]
	v_mfma_f32_16x16x32_f16 v[22:25], v[160:163], v[128:131], v[22:25]
	v_mfma_f32_16x16x32_f16 v[18:21], v[160:163], v[136:139], v[18:21]
	s_setprio 1
	s_setprio 0
	v_mfma_f32_16x16x32_f16 v[10:13], v[62:65], v[98:101], v[10:13]
	v_mfma_f32_16x16x32_f16 v[128:131], v[144:147], v[168:171], v[10:13]
	v_mfma_f32_16x16x32_f16 v[6:9], v[148:151], v[74:77], v[6:9]
	v_mfma_f32_16x16x32_f16 v[2:5], v[148:151], v[98:101], v[2:5]
	v_mfma_f32_16x16x32_f16 v[10:13], v[156:159], v[74:77], v[54:57]
	v_mfma_f32_16x16x32_f16 v[14:17], v[62:65], v[74:77], v[14:17]
	v_mfma_f32_16x16x32_f16 v[6:9], v[152:155], v[78:81], v[6:9]
	v_mfma_f32_16x16x32_f16 v[2:5], v[152:155], v[168:171], v[2:5]
	v_mfma_f32_16x16x32_f16 v[132:135], v[160:163], v[78:81], v[10:13]
	v_mfma_f32_16x16x32_f16 v[10:13], v[156:159], v[98:101], v[58:61]
	v_mfma_f32_16x16x32_f16 v[118:121], v[144:147], v[78:81], v[14:17]
	v_mfma_f32_16x16x32_f16 v[136:139], v[160:163], v[168:171], v[10:13]
	s_setprio 1
	s_barrier
	s_nop 3
	ds_read_b128 v[10:13], v117
	ds_read_b128 v[14:17], v117 offset:1024
	ds_read_b128 v[144:147], v117 offset:2048
	ds_read_b128 v[148:151], v117 offset:3072
	ds_read_b128 v[54:57], v110 offset:24576
	ds_read_b128 v[152:155], v110 offset:25600
	ds_read_b128 v[156:159], v109 offset:24576
	ds_read_b128 v[160:163], v109 offset:25600
	ds_read_b128 v[168:171], v108 offset:24576
	ds_read_b128 v[172:175], v108 offset:25600
	s_waitcnt vmcnt(2)
	s_barrier
	s_waitcnt lgkmcnt(0)
	s_setprio 0
	s_waitcnt lgkmcnt(0)
	v_mfma_f32_16x16x32_f16 v[58:61], v[54:57], v[10:13], v[94:97]
	v_mfma_f32_16x16x32_f16 v[98:101], v[152:155], v[14:17], v[58:61]
	v_mfma_f32_16x16x32_f16 v[58:61], v[54:57], v[144:147], v[90:93]
	v_mfma_f32_16x16x32_f16 v[90:93], v[152:155], v[148:151], v[58:61]
	v_mfma_f32_16x16x32_f16 v[58:61], v[156:159], v[10:13], v[86:89]
	v_mfma_f32_16x16x32_f16 v[78:81], v[160:163], v[14:17], v[58:61]
	v_mfma_f32_16x16x32_f16 v[58:61], v[156:159], v[144:147], v[82:85]
	v_mfma_f32_16x16x32_f16 v[74:77], v[160:163], v[148:151], v[58:61]
	v_mfma_f32_16x16x32_f16 v[58:61], v[168:171], v[10:13], v[124:127]
	v_mfma_f32_16x16x32_f16 v[62:65], v[172:175], v[14:17], v[58:61]
	v_mfma_f32_16x16x32_f16 v[58:61], v[168:171], v[144:147], v[164:167]
	v_mfma_f32_16x16x32_f16 v[58:61], v[172:175], v[148:151], v[58:61]
	s_setprio 1
	s_barrier
	ds_read_b128 v[94:97], v114
	ds_read_b128 v[122:125], v114 offset:1024
	ds_read_b128 v[164:167], v114 offset:2048
	ds_read_b128 v[112:115], v114 offset:3072
	s_waitcnt vmcnt(0)
	s_barrier
	s_waitcnt lgkmcnt(0)
	s_setprio 0
	s_waitcnt lgkmcnt(0)
	v_mfma_f32_16x16x32_f16 v[70:73], v[54:57], v[94:97], v[70:73]
	v_mfma_f32_16x16x32_f16 v[54:57], v[54:57], v[164:167], v[66:69]
	v_mfma_f32_16x16x32_f16 v[82:85], v[152:155], v[112:115], v[54:57]
	v_mfma_f32_16x16x32_f16 v[54:57], v[156:159], v[94:97], v[140:143]
	v_mfma_f32_16x16x32_f16 v[50:53], v[156:159], v[164:167], v[50:53]
	v_mfma_f32_16x16x32_f16 v[46:49], v[168:171], v[94:97], v[46:49]
	v_mfma_f32_16x16x32_f16 v[42:45], v[168:171], v[164:167], v[42:45]
	v_mfma_f32_16x16x32_f16 v[86:89], v[152:155], v[122:125], v[70:73]
	v_mfma_f32_16x16x32_f16 v[70:73], v[160:163], v[122:125], v[54:57]
	v_mfma_f32_16x16x32_f16 v[66:69], v[160:163], v[112:115], v[50:53]
	v_mfma_f32_16x16x32_f16 v[54:57], v[172:175], v[122:125], v[46:49]
	v_mfma_f32_16x16x32_f16 v[50:53], v[172:175], v[112:115], v[42:45]
	s_setprio 1
	s_barrier
	ds_read_b128 v[140:143], v110 offset:36864
	ds_read_b128 v[152:155], v110 offset:37888
	ds_read_b128 v[156:159], v109 offset:36864
	ds_read_b128 v[160:163], v109 offset:37888
	ds_read_b128 v[168:171], v108 offset:36864
	ds_read_b128 v[106:109], v108 offset:37888
	s_barrier
	s_waitcnt lgkmcnt(0)
	s_setprio 0
	s_waitcnt lgkmcnt(0)
	v_mfma_f32_16x16x32_f16 v[38:41], v[140:143], v[10:13], v[38:41]
	v_mfma_f32_16x16x32_f16 v[30:33], v[156:159], v[10:13], v[30:33]
	v_mfma_f32_16x16x32_f16 v[10:13], v[168:171], v[10:13], v[22:25]
	v_mfma_f32_16x16x32_f16 v[46:49], v[152:155], v[14:17], v[38:41]
	v_mfma_f32_16x16x32_f16 v[34:37], v[140:143], v[144:147], v[34:37]
	v_mfma_f32_16x16x32_f16 v[30:33], v[160:163], v[14:17], v[30:33]
	v_mfma_f32_16x16x32_f16 v[26:29], v[156:159], v[144:147], v[26:29]
	v_mfma_f32_16x16x32_f16 v[14:17], v[106:109], v[14:17], v[10:13]
	v_mfma_f32_16x16x32_f16 v[10:13], v[168:171], v[144:147], v[18:21]
	v_mfma_f32_16x16x32_f16 v[42:45], v[152:155], v[148:151], v[34:37]
	v_mfma_f32_16x16x32_f16 v[26:29], v[160:163], v[148:151], v[26:29]
	v_mfma_f32_16x16x32_f16 v[10:13], v[106:109], v[148:151], v[10:13]
	s_setprio 1
	s_setprio 0
	v_mfma_f32_16x16x32_f16 v[18:21], v[140:143], v[94:97], v[118:121]
	v_mfma_f32_16x16x32_f16 v[38:41], v[152:155], v[122:125], v[18:21]
	v_mfma_f32_16x16x32_f16 v[18:21], v[140:143], v[164:167], v[128:131]
	v_mfma_f32_16x16x32_f16 v[2:5], v[156:159], v[164:167], v[2:5]
	v_mfma_f32_16x16x32_f16 v[34:37], v[152:155], v[112:115], v[18:21]
	v_mfma_f32_16x16x32_f16 v[6:9], v[156:159], v[94:97], v[6:9]
	v_mfma_f32_16x16x32_f16 v[18:21], v[160:163], v[112:115], v[2:5]
	v_mfma_f32_16x16x32_f16 v[2:5], v[168:171], v[94:97], v[132:135]
	v_mfma_f32_16x16x32_f16 v[22:25], v[160:163], v[122:125], v[6:9]
	v_mfma_f32_16x16x32_f16 v[6:9], v[106:109], v[122:125], v[2:5]
	v_mfma_f32_16x16x32_f16 v[2:5], v[168:171], v[164:167], v[136:139]
	v_mfma_f32_16x16x32_f16 v[2:5], v[106:109], v[112:115], v[2:5]
	s_setprio 1
	s_andn2_b64 vcc, exec, vcc
	s_barrier
	s_cbranch_vccnz .LBB1_6
	s_barrier
.LBB1_6:
	s_setprio 0
	s_mul_i32 s18, s33, 0xc0
	s_barrier
	v_and_b32_e32 v110, 15, v0
	v_bfe_u32 v111, v0, 4, 2
	s_lshl_b32 s52, s40, 5
	v_or_b32_e32 v112, s52, v110
	v_mul_u32_u24_e32 v113, 0x90, v112
	v_lshl_add_u32 v113, v111, 3, v113
	v_bfe_u32 v114, v0, 2, 1
	v_bfe_u32 v115, v0, 3, 1
	v_lshlrev_b32_e32 v114, 3, v114
	v_lshl_or_b32 v114, v115, 2, v114
	v_and_b32_e32 v115, 3, v0
	v_or_b32_e32 v114, v114, v115
	v_or_b32_e32 v114, s52, v114
	v_lshlrev_b32_e32 v114, 1, v114
	v_mul_u32_u24_e32 v115, 0x840, v111
	v_add_u32_e32 v114, v114, v115
	v_mov_b32_e32 v116, 0x3e38aa3b
	v_mov_b32_e32 v117, 0x3e38aa3b
	s_add_i32 s53, s37, 0
	s_add_i32 s54, s53, s18
	s_lshr_b32 s55, s54, 10
	s_lshr_b32 s56, s53, 6
	s_mul_i32 s56, s56, 0x9000
	s_and_b32 s57, s53, 63
	v_pk_add_f32 v[98:99], v[188:189], v[98:99]
	v_pk_add_f32 v[100:101], v[190:191], v[100:101]
	v_pk_add_f32 v[90:91], v[188:189], v[90:91]
	v_pk_add_f32 v[92:93], v[190:191], v[92:93]
	v_pk_add_f32 v[86:87], v[188:189], v[86:87]
	v_pk_add_f32 v[88:89], v[190:191], v[88:89]
	v_pk_add_f32 v[82:83], v[188:189], v[82:83]
	v_pk_add_f32 v[84:85], v[190:191], v[84:85]
	s_cmp_eq_u32 s55, 2
	s_cbranch_scc1 .Lmy_qe0_v
	s_lshl_b32 s58, s57, 1
	s_add_i32 s58, s58, s56
	v_add_u32_e32 v118, s58, v113
	s_cmp_eq_u32 s55, 0
	s_cbranch_scc0 .Lmy_qe0_ns
	v_pk_mul_f32 v[98:99], v[116:117], v[98:99]
	v_pk_mul_f32 v[100:101], v[116:117], v[100:101]
	v_pk_mul_f32 v[90:91], v[116:117], v[90:91]
	v_pk_mul_f32 v[92:93], v[116:117], v[92:93]
	v_pk_mul_f32 v[86:87], v[116:117], v[86:87]
	v_pk_mul_f32 v[88:89], v[116:117], v[88:89]
	v_pk_mul_f32 v[82:83], v[116:117], v[82:83]
	v_pk_mul_f32 v[84:85], v[116:117], v[84:85]
